# DeltaNet prep: gate cumulative sums via DPP prefix scan (suffix = x + total - prefix) instead of six serial ds_bpermute rounds; on top of attention permlane max, joint query loads and the LRU rebalanc
# speedup vs baseline: 1.0043x; 1.0043x over previous
; __device__ __forceinline__ float lo16(unsigned u) { return __uint_as_float(u << 16); }
; __device__ __forceinline__ float hi16(unsigned u) { return __uint_as_float(u & 0xffff0000u); }
; __device__ void phase_gdn_prep(const Params& p, int l, char* smem, int vb, int nvb, int pend, int oz) {
;     ...
;         {
;             const int t = tid >> 2, qt = tid & 3;
; #pragma unroll
;             for (int which = 0; which < 3; ++which) {
;                 float a[16];
; #pragma unroll
;                 for (int i = 0; i < 16; ++i) a[i] = 0.f;
; #pragma unroll
;                 for (int j = 0; j < 4; ++j) {
;                     const u32x4 x0 = *(const u32x4*)(raw + (t + j) * 192 + which * 64 + qt * 16);
;                     const u32x4 x1 = *(const u32x4*)(raw + (t + j) * 192 + which * 64 + qt * 16 + 8);
;                     const float* cwp = cwl + j * 192 + which * 64 + qt * 16;
; #pragma unroll
;                     for (int w = 0; w < 4; ++w) {
;                         a[2 * w] += cwp[2 * w] * lo16(x0[w]);
;                         a[2 * w + 1] += cwp[2 * w + 1] * hi16(x0[w]);
;                         a[8 + 2 * w] += cwp[8 + 2 * w] * lo16(x1[w]);
;                         a[8 + 2 * w + 1] += cwp[8 + 2 * w + 1] * hi16(x1[w]);
;                     }
;                 }
.LBB0_523:
	s_or_b64 exec, exec, s[0:1]
	v_lshlrev_b32_e32 v2, 5, v8
	v_and_b32_e32 v2, 0x60, v2
	v_lshrrev_b32_e32 v63, 2, v9
	v_add_u32_e32 v64, s81, v2
	s_movk_i32 s0, 0x180
	v_add_u32_e32 v61, v64, v2
	v_mad_u32_u24 v62, v63, s0, v64
	s_waitcnt lgkmcnt(0)
	s_barrier
	ds_read_b128 v[16:19], v62
	ds_read_b128 v[26:29], v62 offset:16
	ds_read_b128 v[12:15], v62 offset:384
	ds_read_b128 v[30:33], v62 offset:400
	ds_read_b128 v[8:11], v62 offset:768
	ds_read_b128 v[34:37], v62 offset:784
	ds_read_b128 v[4:7], v62 offset:1152
	ds_read_b128 v[38:41], v62 offset:1168
	ds_read_b128 v[42:45], v61 offset:53408
	ds_read_b128 v[20:23], v61 offset:53424
	v_and_b32_e32 v2, 64, v236
	ds_read_b128 v[46:49], v61 offset:54192
	ds_read_b128 v[50:53], v61 offset:54176
	v_xor_b32_e32 v24, 1, v236
	v_add_u32_e32 v65, 64, v2
	v_cmp_lt_i32_e32 vcc, v24, v65
	s_waitcnt lgkmcnt(10)
	v_and_b32_e32 v25, 0xffff0000, v29
	s_waitcnt lgkmcnt(6)
	v_lshlrev_b32_e32 v58, 16, v37
	v_cndmask_b32_e32 v66, v236, v24, vcc
	v_lshlrev_b32_e32 v24, 16, v29
	s_waitcnt lgkmcnt(2)
	v_pk_fma_f32 v[22:23], v[22:23], v[24:25], 0 op_sel_hi:[1,1,0]
	v_lshlrev_b32_e32 v24, 16, v33
	v_and_b32_e32 v25, 0xffff0000, v33
	s_waitcnt lgkmcnt(1)
	v_pk_fma_f32 v[48:49], v[48:49], v[24:25], v[22:23]
	ds_read_b128 v[22:25], v61 offset:54960
	ds_read_b128 v[54:57], v61 offset:55728
	ds_read_b128 v[68:71], v61 offset:54944
	v_and_b32_e32 v59, 0xffff0000, v37
	ds_read_b128 v[72:75], v61 offset:55712
	v_lshlrev_b32_e32 v66, 2, v66
	s_waitcnt lgkmcnt(3)
	v_pk_fma_f32 v[24:25], v[24:25], v[58:59], v[48:49]
	v_lshlrev_b32_e32 v48, 16, v41
	v_and_b32_e32 v49, 0xffff0000, v41
	s_waitcnt lgkmcnt(2)
	v_pk_fma_f32 v[24:25], v[56:57], v[48:49], v[24:25]
	v_lshlrev_b32_e32 v48, 16, v28
	v_mul_f32_e32 v29, 0xbfb8aa3b, v24
	v_exp_f32_e32 v29, v29
	v_and_b32_e32 v49, 0xffff0000, v28
	v_pk_fma_f32 v[20:21], v[20:21], v[48:49], 0 op_sel_hi:[1,1,0]
	v_lshlrev_b32_e32 v28, 16, v32
	v_add_f32_e32 v29, 1.0, v29
	v_rcp_f32_e32 v58, v29
	v_and_b32_e32 v29, 0xffff0000, v32
	v_pk_fma_f32 v[20:21], v[46:47], v[28:29], v[20:21]
	v_lshlrev_b32_e32 v28, 16, v36
	v_and_b32_e32 v29, 0xffff0000, v36
	v_pk_fma_f32 v[20:21], v[22:23], v[28:29], v[20:21]
	v_lshlrev_b32_e32 v22, 16, v40
	v_and_b32_e32 v23, 0xffff0000, v40
	v_pk_fma_f32 v[22:23], v[54:55], v[22:23], v[20:21]
	v_mul_f32_e32 v33, 0xbfb8aa3b, v25
	v_mul_f32_e32 v20, 0xbfb8aa3b, v22
	v_exp_f32_e32 v20, v20
	v_mul_f32_e32 v21, 0xbfb8aa3b, v23
	v_exp_f32_e32 v21, v21
	v_exp_f32_e32 v33, v33
	v_add_f32_e32 v20, 1.0, v20
	v_rcp_f32_e32 v28, v20
	v_add_f32_e32 v20, 1.0, v21
	v_rcp_f32_e32 v29, v20
	v_add_f32_e32 v33, 1.0, v33
	v_rcp_f32_e32 v59, v33
	v_lshlrev_b32_e32 v32, 16, v31
	v_pk_mul_f32 v[22:23], v[22:23], v[28:29]
	v_lshlrev_b32_e32 v28, 16, v27
	v_and_b32_e32 v29, 0xffff0000, v27
	v_pk_fma_f32 v[28:29], v[44:45], v[28:29], 0 op_sel_hi:[1,1,0]
	v_and_b32_e32 v33, 0xffff0000, v31
	v_pk_fma_f32 v[28:29], v[52:53], v[32:33], v[28:29]
	v_lshlrev_b32_e32 v32, 16, v35
	v_and_b32_e32 v33, 0xffff0000, v35
	s_waitcnt lgkmcnt(1)
	v_pk_fma_f32 v[28:29], v[70:71], v[32:33], v[28:29]
	v_lshlrev_b32_e32 v32, 16, v39
	v_and_b32_e32 v33, 0xffff0000, v39
	s_waitcnt lgkmcnt(0)
	v_pk_fma_f32 v[32:33], v[74:75], v[32:33], v[28:29]
	v_lshlrev_b32_e32 v40, 16, v26
	v_mul_f32_e32 v27, 0xbfb8aa3b, v32
	v_exp_f32_e32 v27, v27
	v_mul_f32_e32 v28, 0xbfb8aa3b, v33
	v_exp_f32_e32 v31, v28
	v_and_b32_e32 v41, 0xffff0000, v26
	v_add_f32_e32 v27, 1.0, v27
	v_rcp_f32_e32 v36, v27
	v_add_f32_e32 v27, 1.0, v31
	v_rcp_f32_e32 v37, v27
	v_pk_fma_f32 v[26:27], v[42:43], v[40:41], 0 op_sel_hi:[1,1,0]
	v_lshlrev_b32_e32 v40, 16, v30
	v_and_b32_e32 v41, 0xffff0000, v30
	v_pk_fma_f32 v[26:27], v[50:51], v[40:41], v[26:27]
	v_lshlrev_b32_e32 v30, 16, v34
	v_and_b32_e32 v31, 0xffff0000, v34
	v_pk_fma_f32 v[26:27], v[68:69], v[30:31], v[26:27]
	v_lshlrev_b32_e32 v30, 16, v38
	v_and_b32_e32 v31, 0xffff0000, v38
	v_pk_fma_f32 v[30:31], v[72:73], v[30:31], v[26:27]
	ds_read_b128 v[46:49], v61 offset:53376
	ds_read_b128 v[54:57], v61 offset:53392
	v_mul_f32_e32 v26, 0xbfb8aa3b, v30
	v_exp_f32_e32 v34, v26
	v_mul_f32_e32 v26, 0xbfb8aa3b, v31
	v_exp_f32_e32 v35, v26
	ds_read_b128 v[38:41], v61 offset:54160
	ds_read_b128 v[42:45], v61 offset:54144
	ds_read_b128 v[50:53], v61 offset:54928
	v_pk_mul_f32 v[26:27], v[32:33], v[36:37]
	v_add_f32_e32 v32, 1.0, v34
	v_add_f32_e32 v33, 1.0, v35
	v_lshlrev_b32_e32 v34, 16, v19
	v_and_b32_e32 v35, 0xffff0000, v19
	v_pk_mul_f32 v[20:21], v[24:25], v[58:59]
	s_waitcnt lgkmcnt(3)
	v_pk_fma_f32 v[34:35], v[56:57], v[34:35], 0 op_sel_hi:[1,1,0]
	ds_read_b128 v[56:59], v61 offset:55696
	ds_read_b128 v[68:71], v61 offset:54912
	v_lshlrev_b32_e32 v36, 16, v15
	v_and_b32_e32 v37, 0xffff0000, v15
	s_waitcnt lgkmcnt(4)
	v_pk_fma_f32 v[34:35], v[40:41], v[36:37], v[34:35]
	v_lshlrev_b32_e32 v36, 16, v11
	v_and_b32_e32 v37, 0xffff0000, v11
	s_waitcnt lgkmcnt(2)
	v_pk_fma_f32 v[34:35], v[52:53], v[36:37], v[34:35]
	v_lshlrev_b32_e32 v36, 16, v7
	v_and_b32_e32 v37, 0xffff0000, v7
	s_waitcnt lgkmcnt(1)
; __device__ __forceinline__ float siluf_(float x) { return x * __builtin_amdgcn_rcpf(1.f + fexp(-x)); }
; __device__ __forceinline__ float lo16(unsigned u) { return __uint_as_float(u << 16); }
; __device__ __forceinline__ float hi16(unsigned u) { return __uint_as_float(u & 0xffff0000u); }
; __device__ void phase_gdn_prep(const Params& p, int l, char* smem, int vb, int nvb, int pend, int oz) {
;     ...
;             for (int which = 0; which < 3; ++which) {
;                 float a[16];
; #pragma unroll
;                 for (int i = 0; i < 16; ++i) a[i] = 0.f;
; #pragma unroll
;                 for (int j = 0; j < 4; ++j) {
;                     const u32x4 x0 = *(const u32x4*)(raw + (t + j) * 192 + which * 64 + qt * 16);
;                     const u32x4 x1 = *(const u32x4*)(raw + (t + j) * 192 + which * 64 + qt * 16 + 8);
;                     const float* cwp = cwl + j * 192 + which * 64 + qt * 16;
; #pragma unroll
;                     for (int w = 0; w < 4; ++w) {
;                         a[2 * w] += cwp[2 * w] * lo16(x0[w]);
;                         a[2 * w + 1] += cwp[2 * w + 1] * hi16(x0[w]);
;                         a[8 + 2 * w] += cwp[8 + 2 * w] * lo16(x1[w]);
;                         a[8 + 2 * w + 1] += cwp[8 + 2 * w + 1] * hi16(x1[w]);
;                     }
;                 }
;                 float ss = 0.f;
; #pragma unroll
;                 for (int i = 0; i < 16; ++i) {
;                     a[i] = siluf_(a[i]);
;                     ss += a[i] * a[i];
;                 }
	v_pk_fma_f32 v[40:41], v[58:59], v[36:37], v[34:35]
	v_rcp_f32_e32 v32, v32
	v_mul_f32_e32 v7, 0xbfb8aa3b, v40
	v_exp_f32_e32 v7, v7
	v_mul_f32_e32 v11, 0xbfb8aa3b, v41
	v_exp_f32_e32 v11, v11
	v_rcp_f32_e32 v33, v33
	v_add_f32_e32 v7, 1.0, v7
	v_rcp_f32_e32 v52, v7
	v_add_f32_e32 v7, 1.0, v11
	v_rcp_f32_e32 v53, v7
	v_pk_mul_f32 v[30:31], v[30:31], v[32:33]
	ds_read_b128 v[72:75], v61 offset:55680
	v_pk_mul_f32 v[36:37], v[30:31], v[30:31]
	v_pk_mul_f32 v[32:33], v[40:41], v[52:53]
	v_lshlrev_b32_e32 v40, 16, v18
	v_and_b32_e32 v41, 0xffff0000, v18
	v_pk_fma_f32 v[18:19], v[54:55], v[40:41], 0 op_sel_hi:[1,1,0]
	v_lshlrev_b32_e32 v40, 16, v14
	v_and_b32_e32 v41, 0xffff0000, v14
	v_pk_fma_f32 v[14:15], v[38:39], v[40:41], v[18:19]
	v_lshlrev_b32_e32 v18, 16, v10
	v_and_b32_e32 v19, 0xffff0000, v10
	v_pk_fma_f32 v[10:11], v[50:51], v[18:19], v[14:15]
	v_lshlrev_b32_e32 v14, 16, v6
	v_and_b32_e32 v15, 0xffff0000, v6
	v_pk_fma_f32 v[40:41], v[56:57], v[14:15], v[10:11]
	v_lshlrev_b32_e32 v10, 16, v13
	v_mul_f32_e32 v6, 0xbfb8aa3b, v40
	v_exp_f32_e32 v6, v6
	v_mul_f32_e32 v7, 0xbfb8aa3b, v41
	v_exp_f32_e32 v7, v7
	v_and_b32_e32 v11, 0xffff0000, v13
	v_add_f32_e32 v6, 1.0, v6
	v_rcp_f32_e32 v54, v6
	v_add_f32_e32 v14, 1.0, v7
	v_lshlrev_b32_e32 v6, 16, v17
	v_and_b32_e32 v7, 0xffff0000, v17
	v_pk_fma_f32 v[6:7], v[48:49], v[6:7], 0 op_sel_hi:[1,1,0]
	v_rcp_f32_e32 v55, v14
	v_pk_fma_f32 v[6:7], v[44:45], v[10:11], v[6:7]
	v_lshlrev_b32_e32 v10, 16, v9
	v_and_b32_e32 v11, 0xffff0000, v9
	s_waitcnt lgkmcnt(1)
	v_pk_fma_f32 v[6:7], v[70:71], v[10:11], v[6:7]
	v_lshlrev_b32_e32 v10, 16, v5
	v_and_b32_e32 v11, 0xffff0000, v5
	s_waitcnt lgkmcnt(0)
	v_pk_fma_f32 v[48:49], v[74:75], v[10:11], v[6:7]
	v_and_b32_e32 v7, 0xffff0000, v16
	v_mul_f32_e32 v5, 0xbfb8aa3b, v48
	v_exp_f32_e32 v5, v5
	v_mul_f32_e32 v6, 0xbfb8aa3b, v49
	v_exp_f32_e32 v6, v6
	v_lshlrev_b32_e32 v10, 16, v12
	v_add_f32_e32 v5, 1.0, v5
	v_rcp_f32_e32 v132, v5
	v_add_f32_e32 v5, 1.0, v6
	v_lshlrev_b32_e32 v6, 16, v16
	v_pk_fma_f32 v[6:7], v[46:47], v[6:7], 0 op_sel_hi:[1,1,0]
	v_and_b32_e32 v11, 0xffff0000, v12
	v_pk_fma_f32 v[6:7], v[42:43], v[10:11], v[6:7]
	v_lshlrev_b32_e32 v10, 16, v8
	v_and_b32_e32 v11, 0xffff0000, v8
	v_pk_fma_f32 v[6:7], v[68:69], v[10:11], v[6:7]
	v_lshlrev_b32_e32 v8, 16, v4
	v_and_b32_e32 v9, 0xffff0000, v4
	v_pk_fma_f32 v[134:135], v[72:73], v[8:9], v[6:7]
	v_rcp_f32_e32 v133, v5
	v_mul_f32_e32 v4, 0xbfb8aa3b, v134
	v_exp_f32_e32 v4, v4
	v_mul_f32_e32 v6, 0xbfb8aa3b, v135
	v_exp_f32_e32 v6, v6
	v_pk_mul_f32 v[38:39], v[32:33], v[32:33]
	v_add_f32_e32 v4, 1.0, v4
	v_rcp_f32_e32 v136, v4
	v_add_f32_e32 v67, 1.0, v6
	ds_read_b128 v[16:19], v62 offset:128
	ds_read_b128 v[50:53], v62 offset:144
	ds_read_b128 v[12:15], v62 offset:512
	ds_read_b128 v[56:59], v62 offset:528
	ds_read_b128 v[8:11], v62 offset:896
	ds_read_b128 v[68:71], v62 offset:912
	ds_read_b128 v[4:7], v62 offset:1280
	ds_read_b128 v[72:75], v62 offset:1296
	ds_read_b128 v[42:45], v61 offset:53680
	ds_read_b128 v[76:79], v61 offset:54448
	ds_read_b128 v[80:83], v61 offset:53664
	ds_read_b128 v[84:87], v61 offset:54432
	ds_read_b128 v[88:91], v61 offset:55216
	s_waitcnt lgkmcnt(11)
	v_lshlrev_b32_e32 v46, 16, v53
	v_and_b32_e32 v47, 0xffff0000, v53
	ds_read_b128 v[92:95], v61 offset:55984
	ds_read_b128 v[96:99], v61 offset:55200
	s_waitcnt lgkmcnt(6)
	v_pk_fma_f32 v[44:45], v[44:45], v[46:47], 0 op_sel_hi:[1,1,0]
	v_lshlrev_b32_e32 v46, 16, v59
	v_and_b32_e32 v47, 0xffff0000, v59
	s_waitcnt lgkmcnt(5)
	v_pk_fma_f32 v[44:45], v[78:79], v[46:47], v[44:45]
	v_lshlrev_b32_e32 v46, 16, v71
	v_and_b32_e32 v47, 0xffff0000, v71
	s_waitcnt lgkmcnt(2)
	v_pk_fma_f32 v[44:45], v[90:91], v[46:47], v[44:45]
	v_lshlrev_b32_e32 v46, 16, v75
	v_and_b32_e32 v47, 0xffff0000, v75
	s_waitcnt lgkmcnt(1)
	v_pk_fma_f32 v[78:79], v[94:95], v[46:47], v[44:45]
	v_and_b32_e32 v53, 0xffff0000, v58
	v_mul_f32_e32 v44, 0xbfb8aa3b, v78
	v_exp_f32_e32 v44, v44
	v_mul_f32_e32 v45, 0xbfb8aa3b, v79
	v_exp_f32_e32 v45, v45
	ds_read_b128 v[100:103], v61 offset:55968
	v_add_f32_e32 v44, 1.0, v44
	v_rcp_f32_e32 v90, v44
	v_add_f32_e32 v44, 1.0, v45
	v_rcp_f32_e32 v91, v44
	v_pk_mul_f32 v[44:45], v[40:41], v[54:55]
	v_lshlrev_b32_e32 v54, 16, v52
	v_and_b32_e32 v55, 0xffff0000, v52
	v_pk_fma_f32 v[42:43], v[42:43], v[54:55], 0 op_sel_hi:[1,1,0]
	v_lshlrev_b32_e32 v52, 16, v58
	v_pk_fma_f32 v[42:43], v[76:77], v[52:53], v[42:43]
	v_lshlrev_b32_e32 v52, 16, v70
	v_and_b32_e32 v53, 0xffff0000, v70
	v_pk_fma_f32 v[42:43], v[88:89], v[52:53], v[42:43]
	v_lshlrev_b32_e32 v52, 16, v74
	v_and_b32_e32 v53, 0xffff0000, v74
	v_pk_fma_f32 v[42:43], v[92:93], v[52:53], v[42:43]
	v_lshlrev_b32_e32 v58, 16, v51
	v_and_b32_e32 v59, 0xffff0000, v51
	v_mul_f32_e32 v52, 0xbfb8aa3b, v42
	v_mul_f32_e32 v53, 0xbfb8aa3b, v43
	v_pk_fma_f32 v[58:59], v[82:83], v[58:59], 0 op_sel_hi:[1,1,0]
	v_lshlrev_b32_e32 v70, 16, v57
	v_and_b32_e32 v71, 0xffff0000, v57
	v_exp_f32_e32 v52, v52
	v_exp_f32_e32 v53, v53
	v_pk_fma_f32 v[58:59], v[86:87], v[70:71], v[58:59]
	v_lshlrev_b32_e32 v70, 16, v69
	v_and_b32_e32 v71, 0xffff0000, v69
	s_waitcnt lgkmcnt(1)
	v_pk_fma_f32 v[58:59], v[98:99], v[70:71], v[58:59]
	v_lshlrev_b32_e32 v70, 16, v73
	v_and_b32_e32 v71, 0xffff0000, v73
	s_waitcnt lgkmcnt(0)
; __device__ __forceinline__ float siluf_(float x) { return x * __builtin_amdgcn_rcpf(1.f + fexp(-x)); }
; __device__ void phase_gdn_prep(const Params& p, int l, char* smem, int vb, int nvb, int pend, int oz) {
;     ...
;                 float ss = 0.f;
; #pragma unroll
;                 for (int i = 0; i < 16; ++i) {
;                     a[i] = siluf_(a[i]);
;                     ss += a[i] * a[i];
;                 }
;                 float sc = 1.f;
;                 if (which < 2) {
;                     ss += __shfl_xor(ss, 1);
;                     ss += __shfl_xor(ss, 2);
;                     sc = rsqrtf(ss + EPS) * (which == 0 ? 0.125f : 1.f);
	v_pk_fma_f32 v[58:59], v[102:103], v[70:71], v[58:59]
	v_add_f32_e32 v52, 1.0, v52
	v_mul_f32_e32 v51, 0xbfb8aa3b, v58
	v_add_f32_e32 v53, 1.0, v53
	v_exp_f32_e32 v51, v51
	v_rcp_f32_e32 v52, v52
	v_rcp_f32_e32 v53, v53
	v_mul_f32_e32 v57, 0xbfb8aa3b, v59
	v_exp_f32_e32 v57, v57
	v_add_f32_e32 v51, 1.0, v51
	v_lshlrev_b32_e32 v70, 16, v50
	v_and_b32_e32 v71, 0xffff0000, v50
	v_pk_mul_f32 v[42:43], v[42:43], v[52:53]
	v_rcp_f32_e32 v52, v51
	v_pk_fma_f32 v[50:51], v[80:81], v[70:71], 0 op_sel_hi:[1,1,0]
	v_lshlrev_b32_e32 v70, 16, v56
	v_and_b32_e32 v71, 0xffff0000, v56
	v_add_f32_e32 v53, 1.0, v57
	v_pk_fma_f32 v[50:51], v[84:85], v[70:71], v[50:51]
	v_lshlrev_b32_e32 v56, 16, v68
	v_and_b32_e32 v57, 0xffff0000, v68
	v_pk_fma_f32 v[50:51], v[96:97], v[56:57], v[50:51]
	v_lshlrev_b32_e32 v56, 16, v72
	v_and_b32_e32 v57, 0xffff0000, v72
	v_pk_fma_f32 v[68:69], v[100:101], v[56:57], v[50:51]
	v_rcp_f32_e32 v53, v53
	v_mul_f32_e32 v50, 0xbfb8aa3b, v68
	v_exp_f32_e32 v50, v50
	v_mul_f32_e32 v51, 0xbfb8aa3b, v69
	v_exp_f32_e32 v51, v51
	v_pk_mul_f32 v[40:41], v[78:79], v[90:91]
	v_add_f32_e32 v50, 1.0, v50
	v_rcp_f32_e32 v70, v50
	v_add_f32_e32 v50, 1.0, v51
	v_rcp_f32_e32 v71, v50
	v_pk_mul_f32 v[50:51], v[58:59], v[52:53]
	v_lshlrev_b32_e32 v80, 16, v19
	v_and_b32_e32 v81, 0xffff0000, v19
	v_pk_mul_f32 v[52:53], v[68:69], v[70:71]
	ds_read_b128 v[68:71], v61 offset:53648
	ds_read_b128 v[72:75], v61 offset:54416
	ds_read_b128 v[76:79], v61 offset:53632
	v_lshlrev_b32_e32 v84, 16, v15
	v_and_b32_e32 v85, 0xffff0000, v15
	v_rcp_f32_e32 v137, v67
	s_waitcnt lgkmcnt(2)
	v_pk_fma_f32 v[70:71], v[70:71], v[80:81], 0 op_sel_hi:[1,1,0]
	ds_read_b128 v[80:83], v61 offset:54400
	s_waitcnt lgkmcnt(2)
	v_pk_fma_f32 v[70:71], v[74:75], v[84:85], v[70:71]
	ds_read_b128 v[84:87], v61 offset:55184
	ds_read_b128 v[88:91], v61 offset:55952
	ds_read_b128 v[92:95], v61 offset:55168
	v_lshlrev_b32_e32 v74, 16, v11
	v_and_b32_e32 v75, 0xffff0000, v11
	ds_read_b128 v[96:99], v61 offset:55936
	s_waitcnt lgkmcnt(3)
	v_pk_fma_f32 v[70:71], v[86:87], v[74:75], v[70:71]
	v_lshlrev_b32_e32 v74, 16, v7
	v_and_b32_e32 v75, 0xffff0000, v7
	s_waitcnt lgkmcnt(2)
	v_pk_fma_f32 v[70:71], v[90:91], v[74:75], v[70:71]
	v_lshlrev_b32_e32 v90, 16, v18
	v_mul_f32_e32 v7, 0xbfb8aa3b, v70
	v_exp_f32_e32 v7, v7
	v_mul_f32_e32 v11, 0xbfb8aa3b, v71
	v_exp_f32_e32 v11, v11
	v_and_b32_e32 v91, 0xffff0000, v18
	v_pk_fma_f32 v[18:19], v[68:69], v[90:91], 0 op_sel_hi:[1,1,0]
	v_lshlrev_b32_e32 v68, 16, v14
	v_and_b32_e32 v69, 0xffff0000, v14
	v_add_f32_e32 v7, 1.0, v7
	v_pk_fma_f32 v[14:15], v[72:73], v[68:69], v[18:19]
	v_lshlrev_b32_e32 v18, 16, v10
	v_and_b32_e32 v19, 0xffff0000, v10
	v_rcp_f32_e32 v86, v7
	v_add_f32_e32 v7, 1.0, v11
	v_pk_fma_f32 v[10:11], v[84:85], v[18:19], v[14:15]
	v_lshlrev_b32_e32 v18, 16, v17
	v_and_b32_e32 v19, 0xffff0000, v17
	v_pk_fma_f32 v[18:19], v[78:79], v[18:19], 0 op_sel_hi:[1,1,0]
	v_lshlrev_b32_e32 v68, 16, v13
	v_and_b32_e32 v69, 0xffff0000, v13
	v_pk_fma_f32 v[18:19], v[82:83], v[68:69], v[18:19]
	v_lshlrev_b32_e32 v68, 16, v9
	v_and_b32_e32 v69, 0xffff0000, v9
	v_rcp_f32_e32 v87, v7
	s_waitcnt lgkmcnt(1)
	v_pk_fma_f32 v[18:19], v[94:95], v[68:69], v[18:19]
	v_lshlrev_b32_e32 v68, 16, v5
	v_and_b32_e32 v69, 0xffff0000, v5
	s_waitcnt lgkmcnt(0)
	v_pk_fma_f32 v[18:19], v[98:99], v[68:69], v[18:19]
	v_lshlrev_b32_e32 v14, 16, v6
	v_mul_f32_e32 v5, 0xbfb8aa3b, v18
	v_mul_f32_e32 v9, 0xbfb8aa3b, v19
	v_and_b32_e32 v15, 0xffff0000, v6
	v_exp_f32_e32 v5, v5
	v_exp_f32_e32 v9, v9
	v_pk_fma_f32 v[6:7], v[88:89], v[14:15], v[10:11]
	v_pk_mul_f32 v[14:15], v[70:71], v[86:87]
	v_lshlrev_b32_e32 v70, 16, v16
	v_and_b32_e32 v71, 0xffff0000, v16
	v_pk_fma_f32 v[16:17], v[76:77], v[70:71], 0 op_sel_hi:[1,1,0]
	v_lshlrev_b32_e32 v70, 16, v12
	v_and_b32_e32 v71, 0xffff0000, v12
	v_pk_fma_f32 v[12:13], v[80:81], v[70:71], v[16:17]
	v_lshlrev_b32_e32 v16, 16, v8
	v_and_b32_e32 v17, 0xffff0000, v8
	v_add_f32_e32 v5, 1.0, v5
	v_add_f32_e32 v67, 1.0, v9
	v_pk_fma_f32 v[8:9], v[92:93], v[16:17], v[12:13]
	v_lshlrev_b32_e32 v12, 16, v4
	v_and_b32_e32 v13, 0xffff0000, v4
	v_rcp_f32_e32 v68, v5
	v_pk_fma_f32 v[4:5], v[96:97], v[12:13], v[8:9]
	v_mul_f32_e32 v10, 0xbfb8aa3b, v6
	v_mul_f32_e32 v8, 0xbfb8aa3b, v4
	v_mul_f32_e32 v9, 0xbfb8aa3b, v5
	v_exp_f32_e32 v8, v8
	v_exp_f32_e32 v9, v9
	v_mul_f32_e32 v11, 0xbfb8aa3b, v7
	v_exp_f32_e32 v10, v10
	v_exp_f32_e32 v11, v11
	v_add_f32_e32 v8, 1.0, v8
	v_add_f32_e32 v9, 1.0, v9
	v_rcp_f32_e32 v69, v67
	v_rcp_f32_e32 v8, v8
	v_rcp_f32_e32 v9, v9
	v_add_f32_e32 v10, 1.0, v10
	v_add_f32_e32 v11, 1.0, v11
	v_pk_mul_f32 v[46:47], v[48:49], v[132:133]
	v_pk_mul_f32 v[48:49], v[134:135], v[136:137]
	v_rcp_f32_e32 v10, v10
	v_rcp_f32_e32 v11, v11
	v_pk_mul_f32 v[18:19], v[18:19], v[68:69]
	v_pk_mul_f32 v[68:69], v[4:5], v[8:9]
	v_mov_b32_e32 v73, v49
	v_mov_b32_e32 v72, v69
	v_mov_b32_e32 v70, v68
	v_mov_b32_e32 v71, v48
	v_pk_mul_f32 v[72:73], v[72:73], v[72:73]
	v_mov_b32_e32 v8, v18
	v_mov_b32_e32 v9, v46
	v_pk_fma_f32 v[70:71], v[70:71], v[70:71], v[72:73]
	v_pk_mul_f32 v[16:17], v[6:7], v[10:11]
	v_mov_b32_e32 v10, v19
	v_mov_b32_e32 v11, v47
	v_pk_fma_f32 v[8:9], v[8:9], v[8:9], v[70:71]
	v_mov_b32_e32 v4, v16
	v_mov_b32_e32 v5, v44
	v_pk_fma_f32 v[8:9], v[10:11], v[10:11], v[8:9]
	v_pk_mul_f32 v[12:13], v[14:15], v[14:15]
	v_mov_b32_e32 v6, v17
	v_mov_b32_e32 v7, v45
	v_pk_fma_f32 v[4:5], v[4:5], v[4:5], v[8:9]
	v_pk_mul_f32 v[74:75], v[52:53], v[52:53]
	v_pk_fma_f32 v[4:5], v[6:7], v[6:7], v[4:5]
	v_mov_b32_e32 v6, v12
	v_mov_b32_e32 v7, v38
	v_pk_add_f32 v[4:5], v[4:5], v[6:7]
	v_mov_b32_e32 v38, v13
	v_pk_add_f32 v[4:5], v[4:5], v[38:39]
	v_mov_b32_e32 v6, v74
	v_mov_b32_e32 v7, v36
	v_pk_mul_f32 v[34:35], v[26:27], v[26:27]
	v_pk_mul_f32 v[58:59], v[50:51], v[50:51]
	v_pk_add_f32 v[4:5], v[6:7], v[4:5]
	v_mov_b32_e32 v36, v75
	v_pk_add_f32 v[4:5], v[36:37], v[4:5]
	v_mov_b32_e32 v6, v58
	v_mov_b32_e32 v7, v34
	v_pk_mul_f32 v[28:29], v[22:23], v[22:23]
	v_pk_mul_f32 v[56:57], v[42:43], v[42:43]
	v_pk_add_f32 v[4:5], v[6:7], v[4:5]
	v_mov_b32_e32 v34, v59
	v_pk_add_f32 v[4:5], v[34:35], v[4:5]
	v_mov_b32_e32 v6, v56
	v_mov_b32_e32 v7, v28
	v_pk_mul_f32 v[24:25], v[20:21], v[20:21]
	v_pk_mul_f32 v[54:55], v[40:41], v[40:41]
	v_pk_add_f32 v[4:5], v[6:7], v[4:5]
	v_mov_b32_e32 v28, v57
	v_pk_add_f32 v[4:5], v[28:29], v[4:5]
	v_mov_b32_e32 v6, v54
	v_mov_b32_e32 v7, v24
	v_pk_add_f32 v[4:5], v[6:7], v[4:5]
	v_mov_b32_e32 v24, v55
	v_pk_add_f32 v[4:5], v[24:25], v[4:5]
	ds_bpermute_b32 v7, v66, v5
	ds_bpermute_b32 v6, v66, v4
	v_xor_b32_e32 v8, 2, v236
	v_cmp_lt_i32_e32 vcc, v8, v65
	s_mov_b32 s0, 0x358637bd
	s_cmp_gt_i32 s2, 1
	v_cndmask_b32_e32 v8, v236, v8, vcc
	v_lshlrev_b32_e32 v8, 2, v8
	s_waitcnt lgkmcnt(0)
; __device__ void phase_gdn_prep(const Params& p, int l, char* smem, int vb, int nvb, int pend, int oz) {
;     ...
;                 float sc = 1.f;
;                 if (which < 2) {
;                     ss += __shfl_xor(ss, 1);
;                     ss += __shfl_xor(ss, 2);
;                     sc = rsqrtf(ss + EPS) * (which == 0 ? 0.125f : 1.f);
;                 }
;                 bf16_t* dst = (which == 0 ? qs : which == 1 ? ks : vs) + t * LS + qt * 16;
;                 u32x4 o0 = {cvt_pk(a[0] * sc, a[1] * sc), cvt_pk(a[2] * sc, a[3] * sc), cvt_pk(a[4] * sc, a[5] * sc), cvt_pk(a[6] * sc, a[7] * sc)};
;                 u32x4 o1 = {cvt_pk(a[8] * sc, a[9] * sc), cvt_pk(a[10] * sc, a[11] * sc), cvt_pk(a[12] * sc, a[13] * sc), cvt_pk(a[14] * sc, a[15] * sc)};
;                 *(u32x4*)dst = o0;
;                 *(u32x4*)(dst + 8) = o1;
;             }
;         }
	v_pk_add_f32 v[4:5], v[4:5], v[6:7]
	ds_bpermute_b32 v7, v8, v5
	ds_bpermute_b32 v6, v8, v4
	s_waitcnt lgkmcnt(0)
	v_pk_add_f32 v[4:5], v[4:5], v[6:7]
	s_nop 0
	v_pk_add_f32 v[12:13], v[4:5], s[0:1] op_sel_hi:[1,0]
	s_movk_i32 s0, 0x90
	v_mul_f32_e32 v4, 0x4b800000, v13
	v_cmp_gt_f32_e32 vcc, s63, v13
	v_mad_u32_u24 v24, v63, s0, v64
	s_nop 0
	v_cndmask_b32_e32 v4, v13, v4, vcc
	v_rsq_f32_e32 v4, v4
	s_nop 0
	v_mul_f32_e32 v5, 0x45800000, v4
	v_cndmask_b32_e32 v4, v4, v5, vcc
	v_mul_f32_e32 v28, 0x3e000000, v4
	v_pk_mul_f32 v[4:5], v[48:49], v[28:29] op_sel_hi:[1,0]
	v_pk_mul_f32 v[6:7], v[46:47], v[28:29] op_sel_hi:[1,0]
	v_cvt_pk_bf16_f32 v4, v4, v5
	v_cvt_pk_bf16_f32 v5, v6, v7
	v_pk_mul_f32 v[6:7], v[44:45], v[28:29] op_sel_hi:[1,0]
	v_pk_mul_f32 v[8:9], v[32:33], v[28:29] op_sel_hi:[1,0]
	v_cvt_pk_bf16_f32 v6, v6, v7
	v_cvt_pk_bf16_f32 v7, v8, v9
	v_pk_mul_f32 v[8:9], v[30:31], v[28:29] op_sel_hi:[1,0]
	v_pk_mul_f32 v[10:11], v[26:27], v[28:29] op_sel_hi:[1,0]
	v_cvt_pk_bf16_f32 v8, v8, v9
	v_cvt_pk_bf16_f32 v9, v10, v11
	v_pk_mul_f32 v[10:11], v[22:23], v[28:29] op_sel_hi:[1,0]
	v_cmp_gt_f32_e32 vcc, s63, v12
	v_cvt_pk_bf16_f32 v10, v10, v11
	v_mul_f32_e32 v11, 0x4b800000, v12
	v_cndmask_b32_e32 v11, v12, v11, vcc
	v_rsq_f32_e32 v12, v11
	v_pk_mul_f32 v[20:21], v[20:21], v[28:29] op_sel_hi:[1,0]
	s_nop 0
	v_cvt_pk_bf16_f32 v11, v20, v21
	ds_write_b128 v24, v[4:7] offset:25728
	ds_write_b128 v24, v[8:11] offset:25744
	v_mul_f32_e32 v4, 0x45800000, v12
	v_cndmask_b32_e32 v12, v12, v4, vcc
	v_pk_mul_f32 v[4:5], v[68:69], v[12:13] op_sel_hi:[1,0]
	v_pk_mul_f32 v[6:7], v[18:19], v[12:13] op_sel_hi:[1,0]
	v_cvt_pk_bf16_f32 v4, v4, v5
	v_cvt_pk_bf16_f32 v5, v6, v7
	v_pk_mul_f32 v[6:7], v[16:17], v[12:13] op_sel_hi:[1,0]
	v_pk_mul_f32 v[8:9], v[14:15], v[12:13] op_sel_hi:[1,0]
	v_cvt_pk_bf16_f32 v6, v6, v7
	v_cvt_pk_bf16_f32 v7, v8, v9
	v_pk_mul_f32 v[8:9], v[52:53], v[12:13] op_sel_hi:[1,0]
	v_pk_mul_f32 v[10:11], v[50:51], v[12:13] op_sel_hi:[1,0]
	v_cvt_pk_bf16_f32 v8, v8, v9
	v_cvt_pk_bf16_f32 v9, v10, v11
	v_pk_mul_f32 v[10:11], v[42:43], v[12:13] op_sel_hi:[1,0]
	v_pk_mul_f32 v[12:13], v[40:41], v[12:13] op_sel_hi:[1,0]
	v_cvt_pk_bf16_f32 v10, v10, v11
	v_cvt_pk_bf16_f32 v11, v12, v13
	ds_write_b128 v24, v[4:7] offset:34944
	ds_write_b128 v24, v[8:11] offset:34960
	ds_read_b128 v[4:7], v62 offset:256
	ds_read_b128 v[26:29], v62 offset:272
	ds_read_b128 v[30:33], v62 offset:656
	ds_read_b128 v[34:37], v61 offset:53920
	ds_read_b128 v[20:23], v61 offset:53936
	ds_read_b128 v[38:41], v62 offset:1040
	ds_read_b128 v[42:45], v62 offset:1424
	s_waitcnt lgkmcnt(5)
	v_lshlrev_b32_e32 v8, 16, v29
	v_and_b32_e32 v9, 0xffff0000, v29
	s_waitcnt lgkmcnt(2)
	v_pk_fma_f32 v[12:13], v[22:23], v[8:9], 0 op_sel_hi:[1,1,0]
	ds_read_b128 v[46:49], v61 offset:54704
	ds_read_b128 v[8:11], v62 offset:640
	v_lshlrev_b32_e32 v14, 16, v33
	v_and_b32_e32 v15, 0xffff0000, v33
	ds_read_b128 v[50:53], v61 offset:54688
	s_waitcnt lgkmcnt(2)
	v_pk_fma_f32 v[16:17], v[48:49], v[14:15], v[12:13]
	ds_read_b128 v[54:57], v61 offset:55472
	ds_read_b128 v[12:15], v62 offset:1024
	v_lshlrev_b32_e32 v18, 16, v41
	v_and_b32_e32 v19, 0xffff0000, v41
	ds_read_b128 v[64:67], v61 offset:55456
	s_waitcnt lgkmcnt(2)
	v_pk_fma_f32 v[22:23], v[56:57], v[18:19], v[16:17]
	ds_read_b128 v[56:59], v61 offset:56240
	ds_read_b128 v[16:19], v62 offset:1408
	v_lshlrev_b32_e32 v48, 16, v45
	v_and_b32_e32 v49, 0xffff0000, v45
	ds_read_b128 v[68:71], v61 offset:56224
	s_waitcnt lgkmcnt(2)
	v_pk_fma_f32 v[22:23], v[58:59], v[48:49], v[22:23]
	v_lshlrev_b32_e32 v58, 16, v28
	v_mul_f32_e32 v25, 0xbfb8aa3b, v23
	v_exp_f32_e32 v25, v25
	v_mul_f32_e32 v29, 0xbfb8aa3b, v22
	v_exp_f32_e32 v29, v29
	v_and_b32_e32 v59, 0xffff0000, v28
	v_add_f32_e32 v25, 1.0, v25
	v_rcp_f32_e32 v49, v25
	v_add_f32_e32 v25, 1.0, v29
	v_pk_fma_f32 v[20:21], v[20:21], v[58:59], 0 op_sel_hi:[1,1,0]
	v_lshlrev_b32_e32 v28, 16, v32
	v_and_b32_e32 v29, 0xffff0000, v32
	v_pk_fma_f32 v[20:21], v[46:47], v[28:29], v[20:21]
	v_lshlrev_b32_e32 v28, 16, v40
	v_and_b32_e32 v29, 0xffff0000, v40
	v_pk_fma_f32 v[20:21], v[54:55], v[28:29], v[20:21]
	v_lshlrev_b32_e32 v28, 16, v44
	v_and_b32_e32 v29, 0xffff0000, v44
	v_pk_fma_f32 v[28:29], v[56:57], v[28:29], v[20:21]
	v_rcp_f32_e32 v48, v25
	v_mul_f32_e32 v20, 0xbfb8aa3b, v29
	v_exp_f32_e32 v25, v20
	v_mul_f32_e32 v20, 0xbfb8aa3b, v28
	v_exp_f32_e32 v32, v20
	v_pk_mul_f32 v[20:21], v[22:23], v[48:49]
	v_add_f32_e32 v22, 1.0, v25
	v_rcp_f32_e32 v23, v22
	v_add_f32_e32 v22, 1.0, v32
	v_lshlrev_b32_e32 v32, 16, v27
	v_and_b32_e32 v33, 0xffff0000, v27
	v_pk_fma_f32 v[32:33], v[36:37], v[32:33], 0 op_sel_hi:[1,1,0]
	v_lshlrev_b32_e32 v36, 16, v31
	v_and_b32_e32 v37, 0xffff0000, v31
	v_pk_fma_f32 v[32:33], v[52:53], v[36:37], v[32:33]
	v_lshlrev_b32_e32 v36, 16, v39
	v_and_b32_e32 v37, 0xffff0000, v39
	v_pk_fma_f32 v[32:33], v[66:67], v[36:37], v[32:33]
	v_lshlrev_b32_e32 v36, 16, v43
	v_and_b32_e32 v37, 0xffff0000, v43
	s_waitcnt lgkmcnt(0)
; __device__ void phase_gdn_prep(const Params& p, int l, char* smem, int vb, int nvb, int pend, int oz) {
;     ...
;         if (wave < 2) {
;             float v = gl[wave * 64 + lane];
; #pragma unroll
;             for (int off = 1; off < 64; off <<= 1) {
;                 const float nb = wave == 0 ? __shfl_up(v, off) : __shfl_down(v, off);
;                 const bool ok = wave == 0 ? (lane >= off) : (lane + off < 64);
;                 v += ok ? nb : 0.f;
;             }
;             Gl[wave * 64 + lane] = v;
;         }
	v_pk_fma_f32 v[32:33], v[70:71], v[36:37], v[32:33]
	v_rcp_f32_e32 v22, v22
	v_mul_f32_e32 v25, 0xbfb8aa3b, v33
	v_exp_f32_e32 v25, v25
	v_mul_f32_e32 v27, 0xbfb8aa3b, v32
	v_exp_f32_e32 v27, v27
	v_lshlrev_b32_e32 v36, 16, v26
	v_add_f32_e32 v25, 1.0, v25
	v_and_b32_e32 v37, 0xffff0000, v26
	v_pk_mul_f32 v[22:23], v[28:29], v[22:23]
	v_rcp_f32_e32 v29, v25
	v_add_f32_e32 v25, 1.0, v27
	v_pk_fma_f32 v[26:27], v[34:35], v[36:37], 0 op_sel_hi:[1,1,0]
	v_lshlrev_b32_e32 v34, 16, v30
	v_and_b32_e32 v35, 0xffff0000, v30
	v_pk_fma_f32 v[26:27], v[50:51], v[34:35], v[26:27]
	v_lshlrev_b32_e32 v30, 16, v38
	v_and_b32_e32 v31, 0xffff0000, v38
	v_pk_fma_f32 v[26:27], v[64:65], v[30:31], v[26:27]
	v_lshlrev_b32_e32 v30, 16, v42
	v_and_b32_e32 v31, 0xffff0000, v42
	v_pk_fma_f32 v[50:51], v[68:69], v[30:31], v[26:27]
	v_rcp_f32_e32 v28, v25
	v_mul_f32_e32 v25, 0xbfb8aa3b, v51
	v_exp_f32_e32 v25, v25
	v_mul_f32_e32 v26, 0xbfb8aa3b, v50
	v_exp_f32_e32 v26, v26
	ds_read_b128 v[72:75], v61 offset:53888
	ds_read_b128 v[76:79], v61 offset:53904
	v_add_f32_e32 v25, 1.0, v25
	v_pk_mul_f32 v[52:53], v[32:33], v[28:29]
	v_rcp_f32_e32 v55, v25
	v_add_f32_e32 v25, 1.0, v26
	ds_read_b128 v[26:29], v61 offset:54672
	v_lshlrev_b32_e32 v30, 16, v7
	v_and_b32_e32 v31, 0xffff0000, v7
	s_waitcnt lgkmcnt(1)
	v_pk_fma_f32 v[34:35], v[78:79], v[30:31], 0 op_sel_hi:[1,1,0]
	v_lshlrev_b32_e32 v36, 16, v11
	v_and_b32_e32 v37, 0xffff0000, v11
	ds_read_b128 v[30:33], v61 offset:54656
	s_waitcnt lgkmcnt(1)
	v_pk_fma_f32 v[28:29], v[28:29], v[36:37], v[34:35]
	ds_read_b128 v[34:37], v61 offset:55440
	ds_read_b128 v[38:41], v61 offset:56208
	ds_read_b128 v[42:45], v61 offset:55424
	v_lshlrev_b32_e32 v46, 16, v15
	v_and_b32_e32 v47, 0xffff0000, v15
	v_rcp_f32_e32 v54, v25
	s_waitcnt lgkmcnt(2)
	v_pk_fma_f32 v[28:29], v[36:37], v[46:47], v[28:29]
	v_lshlrev_b32_e32 v36, 16, v19
	v_and_b32_e32 v37, 0xffff0000, v19
	s_waitcnt lgkmcnt(1)
	v_pk_fma_f32 v[28:29], v[40:41], v[36:37], v[28:29]
	v_lshlrev_b32_e32 v40, 16, v6
	v_mul_f32_e32 v11, 0xbfb8aa3b, v28
	v_exp_f32_e32 v11, v11
	v_and_b32_e32 v41, 0xffff0000, v6
	v_pk_mul_f32 v[36:37], v[50:51], v[54:55]
	v_pk_fma_f32 v[40:41], v[76:77], v[40:41], 0 op_sel_hi:[1,1,0]
	v_lshlrev_b32_e32 v50, 16, v10
	v_and_b32_e32 v51, 0xffff0000, v10
	v_add_f32_e32 v19, 1.0, v11
	v_pk_fma_f32 v[10:11], v[26:27], v[50:51], v[40:41]
	v_lshlrev_b32_e32 v26, 16, v14
	v_and_b32_e32 v27, 0xffff0000, v14
	v_pk_fma_f32 v[10:11], v[34:35], v[26:27], v[10:11]
	v_lshlrev_b32_e32 v14, 16, v18
	v_and_b32_e32 v15, 0xffff0000, v18
	v_pk_fma_f32 v[10:11], v[38:39], v[14:15], v[10:11]
	ds_read_b128 v[46:49], v61 offset:56192
	v_mul_f32_e32 v6, 0xbfb8aa3b, v11
	v_exp_f32_e32 v14, v6
	v_mul_f32_e32 v6, 0xbfb8aa3b, v10
	v_exp_f32_e32 v18, v6
	v_rcp_f32_e32 v6, v19
	v_add_f32_e32 v14, 1.0, v14
	v_rcp_f32_e32 v15, v14
	v_add_f32_e32 v14, 1.0, v18
	v_lshlrev_b32_e32 v18, 16, v5
	v_and_b32_e32 v19, 0xffff0000, v5
	v_pk_fma_f32 v[18:19], v[74:75], v[18:19], 0 op_sel_hi:[1,1,0]
	v_lshlrev_b32_e32 v26, 16, v9
	v_and_b32_e32 v27, 0xffff0000, v9
	v_pk_fma_f32 v[18:19], v[32:33], v[26:27], v[18:19]
	v_lshlrev_b32_e32 v26, 16, v13
	v_and_b32_e32 v27, 0xffff0000, v13
	s_waitcnt lgkmcnt(1)
	v_pk_fma_f32 v[18:19], v[44:45], v[26:27], v[18:19]
	v_lshlrev_b32_e32 v26, 16, v17
	v_and_b32_e32 v27, 0xffff0000, v17
	s_waitcnt lgkmcnt(0)
	v_pk_fma_f32 v[18:19], v[48:49], v[26:27], v[18:19]
	v_lshlrev_b32_e32 v26, 16, v4
	v_mul_f32_e32 v9, 0xbfb8aa3b, v18
	v_exp_f32_e32 v9, v9
	v_and_b32_e32 v27, 0xffff0000, v4
	v_pk_fma_f32 v[26:27], v[72:73], v[26:27], 0 op_sel_hi:[1,1,0]
	v_lshlrev_b32_e32 v32, 16, v8
	v_and_b32_e32 v33, 0xffff0000, v8
	v_add_f32_e32 v17, 1.0, v9
	v_pk_fma_f32 v[8:9], v[30:31], v[32:33], v[26:27]
	v_lshlrev_b32_e32 v26, 16, v12
	v_and_b32_e32 v27, 0xffff0000, v12
	v_pk_fma_f32 v[8:9], v[42:43], v[26:27], v[8:9]
	v_lshlrev_b32_e32 v12, 16, v16
	v_and_b32_e32 v13, 0xffff0000, v16
	v_pk_fma_f32 v[8:9], v[46:47], v[12:13], v[8:9]
	v_mul_f32_e32 v7, 0xbfb8aa3b, v29
	v_mul_f32_e32 v4, 0xbfb8aa3b, v9
	v_mul_f32_e32 v5, 0xbfb8aa3b, v19
	v_exp_f32_e32 v12, v4
	v_mul_f32_e32 v4, 0xbfb8aa3b, v8
	v_exp_f32_e32 v7, v7
	v_exp_f32_e32 v5, v5
	v_exp_f32_e32 v16, v4
	v_add_f32_e32 v12, 1.0, v12
	v_add_f32_e32 v7, 1.0, v7
	v_add_f32_e32 v5, 1.0, v5
	v_rcp_f32_e32 v13, v12
	v_add_f32_e32 v12, 1.0, v16
	v_rcp_f32_e32 v7, v7
	v_rcp_f32_e32 v14, v14
	v_rcp_f32_e32 v5, v5
	v_rcp_f32_e32 v4, v17
	v_rcp_f32_e32 v12, v12
	v_pk_mul_f32 v[16:17], v[28:29], v[6:7]
	v_pk_mul_f32 v[6:7], v[10:11], v[14:15]
	v_pk_mul_f32 v[10:11], v[18:19], v[4:5]
	v_pk_mul_f32 v[4:5], v[8:9], v[12:13]
	v_cvt_pk_bf16_f32 v6, v6, v7
	v_cvt_pk_bf16_f32 v4, v4, v5
	v_cvt_pk_bf16_f32 v5, v10, v11
	v_cvt_pk_bf16_f32 v7, v16, v17
	v_cvt_pk_bf16_f32 v8, v36, v37
	v_cvt_pk_bf16_f32 v9, v52, v53
	v_cvt_pk_bf16_f32 v10, v22, v23
	v_cvt_pk_bf16_f32 v11, v20, v21
	ds_write_b128 v24, v[4:7] offset:44160
	ds_write_b128 v24, v[8:11] offset:44176
	s_cbranch_scc1 .LBB0_549
	v_lshlrev_b32_e32 v4, 2, v60
	v_lshl_or_b32 v4, s2, 8, v4
	v_add_u32_e32 v4, s81, v4
	ds_read_b32 v5, v4 offset:56448
	s_waitcnt lgkmcnt(0)
	v_mov_b32_e32 v6, v5
	s_nop 1
	v_add_f32_dpp v6, v5, v6 row_shr:1 row_mask:0xf bank_mask:0xf
	v_add_f32_dpp v6, v5, v6 row_shr:2 row_mask:0xf bank_mask:0xf
	v_add_f32_dpp v6, v5, v6 row_shr:3 row_mask:0xf bank_mask:0xf
	s_nop 1
	v_add_f32_dpp v6, v6, v6 row_shr:4 row_mask:0xf bank_mask:0xe
	s_nop 1
	v_add_f32_dpp v6, v6, v6 row_shr:8 row_mask:0xf bank_mask:0xc
	s_nop 1
	v_add_f32_dpp v6, v6, v6 row_bcast:15 row_mask:0xa bank_mask:0xf
	s_nop 1
	v_add_f32_dpp v6, v6, v6 row_bcast:31 row_mask:0xc bank_mask:0xf
	s_cmp_eq_u32 s2, 0
	s_cbranch_scc1 .Lgp_cs_fwd
	s_nop 0
	v_readlane_b32 s0, v6, 63
	s_nop 1
	v_sub_f32_e32 v6, s0, v6
	v_add_f32_e32 v6, v5, v6
.Lgp_cs_fwd:
	ds_write_b32 v4, v6 offset:57472
